# counted waits: in-projection K-loop's first two waits after an epilogue use vmcnt(24) so they no longer wait for the epilogue's 16 output stores to be acknowledged
# baseline (speedup 1.0000x reference)
.LBB0_273:
	s_mov_b32 s36, 0
	v_bfe_i32 v3, v5, 27, 1
	v_lshlrev_b32_e32 v1, 4, v5
	v_lshrrev_b32_e32 v3, 22, v3
	v_ashrrev_i32_e32 v2, 31, v5
	v_add_u32_e32 v3, v1, v3
	v_lshrrev_b32_e32 v2, 26, v2
	v_and_b32_e32 v3, 0xfffffc00, v3
	v_add_u32_e32 v2, v5, v2
	v_sub_u32_e32 v3, v1, v3
	v_ashrrev_i32_e32 v2, 6, v2
	v_lshrrev_b32_e32 v4, 4, v3
	v_bitop3_b32 v4, v4, v3, 32 bitop3:0x6c
	v_lshlrev_b32_e32 v3, 3, v2
	v_and_b32_e32 v6, -16, v3
	v_ashrrev_i32_e32 v3, 31, v4
	v_lshrrev_b32_e32 v3, 26, v3
	v_add_u32_e32 v7, v4, v3
	v_ashrrev_i32_e32 v3, 6, v7
	v_and_b32_e32 v7, 0xc0, v7
	v_readlane_b32 s0, v254, 51
	v_sub_u32_e32 v4, v4, v7
	s_bitcmp1_b32 s0, 0
	s_mov_b32 s0, 0x7161000
	v_lshlrev_b32_e32 v8, 5, v2
	v_ashrrev_i16_sdwa v4, v226, sext(v4) dst_sel:DWORD dst_unused:UNUSED_PAD src0_sel:DWORD src1_sel:BYTE_0
	s_cselect_b32 s0, s0, 0xa71000
	v_and_b32_e32 v8, 32, v8
	v_bfe_i32 v4, v4, 0, 16
	s_add_u32 s2, s74, s0
	v_add_u32_e32 v6, v3, v6
	v_and_b32_e32 v10, 3, v3
	s_mov_b32 s0, 0x1fffe0
	v_add_lshl_u32 v8, v8, v4, 1
	v_add_u32_e32 v1, 0x2000, v1
	v_lshlrev_b32_e32 v7, 1, v6
	v_lshrrev_b32_e32 v9, 2, v6
	v_and_or_b32 v10, v6, s0, v10
	v_lshl_add_u32 v196, v6, 11, v8
	v_ashrrev_i32_e32 v6, 31, v1
	v_lshrrev_b32_e32 v6, 22, v6
	v_and_b32_e32 v7, 24, v7
	v_and_b32_e32 v9, 4, v9
	v_add_u32_e32 v6, v1, v6
	v_or3_b32 v7, v10, v9, v7
	v_ashrrev_i32_e32 v6, 10, v6
	v_lshl_add_u32 v198, v7, 11, v8
	v_mul_i32_i24_e32 v7, 0x400, v6
	v_sub_u32_e32 v1, v1, v7
	v_lshrrev_b32_e32 v7, 4, v1
	v_bitop3_b32 v1, v7, v1, 32 bitop3:0x6c
	v_lshlrev_b32_e32 v7, 3, v6
	v_and_b32_e32 v8, -16, v7
	v_ashrrev_i32_e32 v7, 31, v1
	v_lshrrev_b32_e32 v7, 26, v7
	v_add_u32_e32 v9, v1, v7
	v_ashrrev_i32_e32 v7, 6, v9
	v_add_u32_e32 v10, v7, v8
	v_lshlrev_b32_e32 v8, 5, v6
	s_addc_u32 s3, s75, 0
	v_and_b32_e32 v11, 32, v8
	v_and_b32_e32 v8, 0xc0, v9
	v_and_b32_e32 v12, 3, v7
	s_ashr_i32 s20, s18, 6
	s_ashr_i32 s17, s16, 31
	s_ashr_i32 s15, s14, 31
	s_ashr_i32 s19, s18, 8
	v_sub_u32_e32 v1, v1, v8
	v_and_or_b32 v12, v10, s0, v12
	s_lshl_b32 s21, s20, 10
	s_lshl_b64 s[12:13], s[16:17], 19
	s_lshl_b64 s[0:1], s[14:15], 19
	v_ashrrev_i16_sdwa v1, v226, sext(v1) dst_sel:DWORD dst_unused:UNUSED_PAD src0_sel:DWORD src1_sel:BYTE_0
	s_add_u32 s0, s2, s0
	v_bfe_i32 v8, v1, 0, 16
	v_lshlrev_b32_e32 v1, 1, v10
	v_lshrrev_b32_e32 v9, 2, v10
	s_addc_u32 s1, s3, s1
	s_add_i32 s15, s21, 0
	v_and_b32_e32 v1, 24, v1
	v_and_b32_e32 v9, 4, v9
	s_add_i32 s17, s15, 0x10000
	s_add_i32 s42, s15, 0x12000
	v_or3_b32 v1, v12, v9, v1
	v_add_lshl_u32 v9, v11, v8, 1
	s_mov_b32 m0, s17
	s_add_u32 s22, s0, 0x40000
	v_lshl_add_u32 v202, v1, 11, v9
	global_load_lds_dwordx4 v198, s[0:1]
	s_mov_b32 m0, s42
	s_addc_u32 s23, s1, 0
	s_add_i32 s43, s15, 0x14000
	s_add_i32 s44, s15, 0x16000
	global_load_lds_dwordx4 v202, s[0:1]
	s_mov_b32 m0, s43
	s_add_u32 s34, s58, s12
	global_load_lds_dwordx4 v198, s[22:23]
	s_mov_b32 m0, s44
	s_addc_u32 s35, s59, s13
	s_add_i32 s45, s15, 0x2000
	global_load_lds_dwordx4 v202, s[22:23]
	s_mov_b32 m0, s15
	s_add_u32 s12, s34, 0x40000
	v_lshl_add_u32 v200, v10, 11, v9
	global_load_lds_dwordx4 v196, s[34:35]
	s_mov_b32 m0, s45
	s_addc_u32 s13, s35, 0
	s_add_i32 s46, s15, 0x4000
	global_load_lds_dwordx4 v200, s[34:35]
	s_mov_b32 m0, s46
	s_add_i32 s47, s15, 0x6000
	global_load_lds_dwordx4 v196, s[12:13]
	s_mov_b32 m0, s47
	s_cmp_eq_u32 s19, 1
	global_load_lds_dwordx4 v200, s[12:13]
	s_cselect_b64 s[12:13], -1, 0
	s_cmp_lg_u32 s19, 1
	s_cbranch_scc1 .LBB0_275
	s_barrier

.LBB0_289:
	v_add_u32_e32 v114, 0x10000, v217
	ds_read_b128 v[148:151], v114
	ds_read_b128 v[152:155], v114 offset:1024
	ds_read_b128 v[156:159], v114 offset:2048
	ds_read_b128 v[160:163], v114 offset:3072
	v_add_u32_e32 v114, 0x14000, v217
	ds_read_b128 v[132:135], v114
	ds_read_b128 v[136:139], v114 offset:1024
	ds_read_b128 v[140:143], v114 offset:2048
	ds_read_b128 v[144:147], v114 offset:3072
	v_lshl_add_u64 v[208:209], s[34:35], 0, v[204:205]
	s_add_i32 m0, s15, 0xc000
	ds_read_b128 v[188:191], v218
	ds_read_b128 v[192:195], v218 offset:1024
	ds_read_b128 v[180:183], v218 offset:2048
	ds_read_b128 v[184:187], v218 offset:3072
	ds_read_b128 v[172:175], v218 offset:4096
	ds_read_b128 v[176:179], v218 offset:5120
	ds_read_b128 v[164:167], v218 offset:6144
	ds_read_b128 v[168:171], v218 offset:7168
	global_load_lds_dwordx4 v[208:209], off
	v_lshl_add_u64 v[208:209], s[34:35], 0, v[206:207]
	s_add_i32 m0, s15, 0xe000
	s_nop 0
	global_load_lds_dwordx4 v[208:209], off
	s_cmp_eq_u32 s36, 1
	s_cbranch_scc0 .Lw3_s0
	s_waitcnt vmcnt(24)
	s_branch .Lw3_j0
.Lw3_s0:
	s_waitcnt vmcnt(8)
.Lw3_j0:
	s_waitcnt lgkmcnt(0)
	s_barrier
	s_setprio 1
	s_waitcnt lgkmcnt(0)
	v_mfma_f32_16x16x32_bf16 v[128:131], v[148:151], v[188:191], v[128:131]
	v_mfma_f32_16x16x32_bf16 v[124:127], v[156:159], v[188:191], v[124:127]
	v_mfma_f32_16x16x32_bf16 v[120:123], v[148:151], v[180:183], v[120:123]
	v_mfma_f32_16x16x32_bf16 v[116:119], v[156:159], v[180:183], v[116:119]
	v_mfma_f32_16x16x32_bf16 v[110:113], v[148:151], v[172:175], v[110:113]
	v_mfma_f32_16x16x32_bf16 v[106:109], v[156:159], v[172:175], v[106:109]
	v_mfma_f32_16x16x32_bf16 v[102:105], v[148:151], v[164:167], v[102:105]
	v_mfma_f32_16x16x32_bf16 v[98:101], v[156:159], v[164:167], v[98:101]
	v_mfma_f32_16x16x32_bf16 v[128:131], v[152:155], v[192:195], v[128:131]
	v_mfma_f32_16x16x32_bf16 v[124:127], v[160:163], v[192:195], v[124:127]
	v_mfma_f32_16x16x32_bf16 v[120:123], v[152:155], v[184:187], v[120:123]
	v_mfma_f32_16x16x32_bf16 v[116:119], v[160:163], v[184:187], v[116:119]
	v_mfma_f32_16x16x32_bf16 v[110:113], v[152:155], v[176:179], v[110:113]
	v_mfma_f32_16x16x32_bf16 v[106:109], v[160:163], v[176:179], v[106:109]
	v_mfma_f32_16x16x32_bf16 v[102:105], v[152:155], v[168:171], v[102:105]
	v_mfma_f32_16x16x32_bf16 v[98:101], v[160:163], v[168:171], v[98:101]
	s_setprio 0
	v_cndmask_b32_e64 v114, 0, 1, s[30:31]
	v_cmp_ne_u32_e64 s[0:1], 1, v114
	s_andn2_b64 vcc, exec, s[30:31]
	s_cbranch_vccnz .LBB0_291
	s_setprio 1
	v_mfma_f32_16x16x32_bf16 v[62:65], v[132:135], v[188:191], v[62:65]
	v_mfma_f32_16x16x32_bf16 v[58:61], v[140:143], v[188:191], v[58:61]
	v_mfma_f32_16x16x32_bf16 v[54:57], v[132:135], v[180:183], v[54:57]
	v_mfma_f32_16x16x32_bf16 v[50:53], v[140:143], v[180:183], v[50:53]
	v_mfma_f32_16x16x32_bf16 v[46:49], v[132:135], v[172:175], v[46:49]
	v_mfma_f32_16x16x32_bf16 v[42:45], v[140:143], v[172:175], v[42:45]
	v_mfma_f32_16x16x32_bf16 v[38:41], v[132:135], v[164:167], v[38:41]
	v_mfma_f32_16x16x32_bf16 v[34:37], v[140:143], v[164:167], v[34:37]
	v_mfma_f32_16x16x32_bf16 v[62:65], v[136:139], v[192:195], v[62:65]
	v_mfma_f32_16x16x32_bf16 v[58:61], v[144:147], v[192:195], v[58:61]
	v_mfma_f32_16x16x32_bf16 v[54:57], v[136:139], v[184:187], v[54:57]
	v_mfma_f32_16x16x32_bf16 v[50:53], v[144:147], v[184:187], v[50:53]
	v_mfma_f32_16x16x32_bf16 v[46:49], v[136:139], v[176:179], v[46:49]
	v_mfma_f32_16x16x32_bf16 v[42:45], v[144:147], v[176:179], v[42:45]
	v_mfma_f32_16x16x32_bf16 v[38:41], v[136:139], v[168:171], v[38:41]
	v_mfma_f32_16x16x32_bf16 v[34:37], v[144:147], v[168:171], v[34:37]
	s_setprio 0
.LBB0_291:
	s_add_u32 s38, s34, 0xfffc0080
	s_addc_u32 s39, s35, -1
	s_cmp_eq_u32 s80, 12
	s_cselect_b32 s41, s23, s39
	s_cselect_b32 s40, s56, s38
	s_cselect_b32 s39, s21, s77
	s_cselect_b32 s38, s57, s76
	s_barrier
	s_mov_b32 m0, s17
	v_lshl_add_u64 v[208:209], s[38:39], 0, v[198:199]
	s_add_u32 s88, s38, 0x40000
	ds_read_b128 v[188:191], v218 offset:16384
	ds_read_b128 v[192:195], v218 offset:17408
	ds_read_b128 v[180:183], v218 offset:18432
	ds_read_b128 v[184:187], v218 offset:19456
	ds_read_b128 v[172:175], v218 offset:20480
	ds_read_b128 v[176:179], v218 offset:21504
	ds_read_b128 v[164:167], v218 offset:22528
	ds_read_b128 v[168:171], v218 offset:23552
	global_load_lds_dwordx4 v[208:209], off
	v_lshl_add_u64 v[210:211], s[38:39], 0, v[202:203]
	s_mov_b32 m0, s42
	s_addc_u32 s89, s39, 0
	global_load_lds_dwordx4 v[210:211], off
	v_lshl_add_u64 v[212:213], s[88:89], 0, v[198:199]
	s_mov_b32 m0, s43
	v_lshl_add_u64 v[214:215], s[40:41], 0, v[200:201]
	global_load_lds_dwordx4 v[212:213], off
	v_lshl_add_u64 v[212:213], s[88:89], 0, v[202:203]
	s_mov_b32 m0, s44
	s_nop 0
	global_load_lds_dwordx4 v[212:213], off
	v_lshl_add_u64 v[212:213], s[40:41], 0, v[196:197]
	s_mov_b32 m0, s15
	s_nop 0
	global_load_lds_dwordx4 v[212:213], off
	s_mov_b32 m0, s45
	s_nop 0
	global_load_lds_dwordx4 v[214:215], off
	s_cmp_eq_u32 s36, 1
	s_cbranch_scc0 .Lw3_s1
	s_waitcnt vmcnt(24)
	s_branch .Lw3_j1

.Lw3_j1:
	s_mov_b32 s36, 0
	s_waitcnt lgkmcnt(0)
	s_barrier
	s_setprio 1
	s_waitcnt lgkmcnt(0)
	v_mfma_f32_16x16x32_bf16 v[94:97], v[148:151], v[188:191], v[94:97]
	v_mfma_f32_16x16x32_bf16 v[90:93], v[156:159], v[188:191], v[90:93]
	v_mfma_f32_16x16x32_bf16 v[86:89], v[148:151], v[180:183], v[86:89]
	v_mfma_f32_16x16x32_bf16 v[82:85], v[156:159], v[180:183], v[82:85]
	v_mfma_f32_16x16x32_bf16 v[78:81], v[148:151], v[172:175], v[78:81]
	v_mfma_f32_16x16x32_bf16 v[74:77], v[156:159], v[172:175], v[74:77]
	v_mfma_f32_16x16x32_bf16 v[70:73], v[148:151], v[164:167], v[70:73]
	v_mfma_f32_16x16x32_bf16 v[66:69], v[156:159], v[164:167], v[66:69]
	v_mfma_f32_16x16x32_bf16 v[94:97], v[152:155], v[192:195], v[94:97]
	v_mfma_f32_16x16x32_bf16 v[90:93], v[160:163], v[192:195], v[90:93]
	v_mfma_f32_16x16x32_bf16 v[86:89], v[152:155], v[184:187], v[86:89]
	v_mfma_f32_16x16x32_bf16 v[82:85], v[160:163], v[184:187], v[82:85]
	v_mfma_f32_16x16x32_bf16 v[78:81], v[152:155], v[176:179], v[78:81]
	v_mfma_f32_16x16x32_bf16 v[74:77], v[160:163], v[176:179], v[74:77]
	v_mfma_f32_16x16x32_bf16 v[70:73], v[152:155], v[168:171], v[70:73]
	v_mfma_f32_16x16x32_bf16 v[66:69], v[160:163], v[168:171], v[66:69]
	s_setprio 0
	s_and_b64 vcc, exec, s[0:1]
	s_cbranch_vccnz .LBB0_293
	s_setprio 1
	v_mfma_f32_16x16x32_bf16 v[30:33], v[132:135], v[188:191], v[30:33]
	v_mfma_f32_16x16x32_bf16 v[26:29], v[140:143], v[188:191], v[26:29]
	v_mfma_f32_16x16x32_bf16 v[22:25], v[132:135], v[180:183], v[22:25]
	v_mfma_f32_16x16x32_bf16 v[18:21], v[140:143], v[180:183], v[18:21]
	v_mfma_f32_16x16x32_bf16 v[14:17], v[132:135], v[172:175], v[14:17]
	v_mfma_f32_16x16x32_bf16 v[10:13], v[140:143], v[172:175], v[10:13]
	v_mfma_f32_16x16x32_bf16 v[6:9], v[132:135], v[164:167], v[6:9]
	v_mfma_f32_16x16x32_bf16 v[2:5], v[140:143], v[164:167], v[2:5]
	v_mfma_f32_16x16x32_bf16 v[30:33], v[136:139], v[192:195], v[30:33]
	v_mfma_f32_16x16x32_bf16 v[26:29], v[144:147], v[192:195], v[26:29]
	v_mfma_f32_16x16x32_bf16 v[22:25], v[136:139], v[184:187], v[22:25]
	v_mfma_f32_16x16x32_bf16 v[18:21], v[144:147], v[184:187], v[18:21]
	v_mfma_f32_16x16x32_bf16 v[14:17], v[136:139], v[176:179], v[14:17]
	v_mfma_f32_16x16x32_bf16 v[10:13], v[144:147], v[176:179], v[10:13]
	v_mfma_f32_16x16x32_bf16 v[6:9], v[136:139], v[168:171], v[6:9]
	v_mfma_f32_16x16x32_bf16 v[2:5], v[144:147], v[168:171], v[2:5]
	s_setprio 0

.LBB0_299:
	v_lshl_or_b32 v132, s14, 8, v216
	v_lshl_add_u32 v114, s16, 8, v1
	v_ashrrev_i32_e32 v133, 31, v132
	v_mov_b64_e32 v[134:135], s[10:11]
	v_mad_i64_i32 v[136:137], s[0:1], v114, s96, v[134:135]
	v_lshlrev_b64 v[132:133], 1, v[132:133]
	v_cvt_pk_bf16_f32 v62, v62, v63
	v_cvt_pk_bf16_f32 v63, v64, v65
	v_cvt_pk_bf16_f32 v64, v58, v59
	v_or_b32_e32 v58, 16, v114
	v_lshl_add_u64 v[136:137], v[136:137], 0, v[132:133]
	v_cvt_pk_bf16_f32 v65, v60, v61
	v_mad_i64_i32 v[58:59], s[0:1], v58, s96, v[134:135]
	v_cvt_pk_bf16_f32 v54, v54, v55
	v_cvt_pk_bf16_f32 v55, v56, v57
	v_cvt_pk_bf16_f32 v56, v50, v51
	v_or_b32_e32 v50, 32, v114
	global_store_dwordx4 v[136:137], v[62:65], off offset:256
	v_cvt_pk_bf16_f32 v57, v52, v53
	v_mad_i64_i32 v[50:51], s[0:1], v50, s96, v[134:135]
	v_lshl_add_u64 v[62:63], v[58:59], 0, v[132:133]
	v_cvt_pk_bf16_f32 v46, v46, v47
	v_cvt_pk_bf16_f32 v47, v48, v49
	v_cvt_pk_bf16_f32 v48, v42, v43
	v_or_b32_e32 v42, 48, v114
	global_store_dwordx4 v[62:63], v[54:57], off offset:256
	v_cvt_pk_bf16_f32 v49, v44, v45
	v_mad_i64_i32 v[42:43], s[0:1], v42, s96, v[134:135]
	v_lshl_add_u64 v[54:55], v[50:51], 0, v[132:133]
	v_cvt_pk_bf16_f32 v38, v38, v39
	v_cvt_pk_bf16_f32 v39, v40, v41
	v_cvt_pk_bf16_f32 v40, v34, v35
	v_add_u32_e32 v34, 0x80, v114
	global_store_dwordx4 v[54:55], v[46:49], off offset:256
	v_cvt_pk_bf16_f32 v41, v36, v37
	v_mad_i64_i32 v[34:35], s[0:1], v34, s96, v[134:135]
	v_lshl_add_u64 v[46:47], v[42:43], 0, v[132:133]
	v_cvt_pk_bf16_f32 v30, v30, v31
	v_cvt_pk_bf16_f32 v31, v32, v33
	v_cvt_pk_bf16_f32 v32, v26, v27
	v_add_u32_e32 v26, 0x90, v114
	global_store_dwordx4 v[46:47], v[38:41], off offset:256
	v_cvt_pk_bf16_f32 v33, v28, v29
	v_mad_i64_i32 v[26:27], s[0:1], v26, s96, v[134:135]
	v_lshl_add_u64 v[38:39], v[34:35], 0, v[132:133]
	v_cvt_pk_bf16_f32 v22, v22, v23
	v_cvt_pk_bf16_f32 v23, v24, v25
	v_cvt_pk_bf16_f32 v24, v18, v19
	v_add_u32_e32 v18, 0xa0, v114
	global_store_dwordx4 v[38:39], v[30:33], off offset:256
	v_cvt_pk_bf16_f32 v25, v20, v21
	v_mad_i64_i32 v[18:19], s[0:1], v18, s96, v[134:135]
	v_lshl_add_u64 v[30:31], v[26:27], 0, v[132:133]
	v_cvt_pk_bf16_f32 v14, v14, v15
	v_cvt_pk_bf16_f32 v15, v16, v17
	v_cvt_pk_bf16_f32 v16, v10, v11
	v_add_u32_e32 v10, 0xb0, v114
	global_store_dwordx4 v[30:31], v[22:25], off offset:256
	v_cvt_pk_bf16_f32 v17, v12, v13
	v_mad_i64_i32 v[10:11], s[0:1], v10, s96, v[134:135]
	v_lshl_add_u64 v[22:23], v[18:19], 0, v[132:133]
	v_readlane_b32 s76, v254, 60
	v_cvt_pk_bf16_f32 v128, v128, v129
	v_cvt_pk_bf16_f32 v129, v130, v131
	v_cvt_pk_bf16_f32 v130, v124, v125
	v_cvt_pk_bf16_f32 v131, v126, v127
	v_cvt_pk_bf16_f32 v58, v120, v121
	v_cvt_pk_bf16_f32 v59, v122, v123
	v_cvt_pk_bf16_f32 v60, v116, v117
	v_cvt_pk_bf16_f32 v61, v118, v119
	v_cvt_pk_bf16_f32 v50, v110, v111
	v_cvt_pk_bf16_f32 v51, v112, v113
	v_cvt_pk_bf16_f32 v52, v106, v107
	v_cvt_pk_bf16_f32 v53, v108, v109
	v_cvt_pk_bf16_f32 v42, v102, v103
	v_cvt_pk_bf16_f32 v43, v104, v105
	v_cvt_pk_bf16_f32 v44, v98, v99
	v_cvt_pk_bf16_f32 v45, v100, v101
	v_cvt_pk_bf16_f32 v34, v94, v95
	v_cvt_pk_bf16_f32 v35, v96, v97
	v_cvt_pk_bf16_f32 v36, v90, v91
	v_cvt_pk_bf16_f32 v37, v92, v93
	v_cvt_pk_bf16_f32 v26, v86, v87
	v_cvt_pk_bf16_f32 v27, v88, v89
	v_cvt_pk_bf16_f32 v28, v82, v83
	v_cvt_pk_bf16_f32 v29, v84, v85
	v_cvt_pk_bf16_f32 v18, v78, v79
	v_cvt_pk_bf16_f32 v19, v80, v81
	v_cvt_pk_bf16_f32 v20, v74, v75
	v_cvt_pk_bf16_f32 v21, v76, v77
	global_store_dwordx4 v[22:23], v[14:17], off offset:256
	v_cvt_pk_bf16_f32 v12, v66, v67
	v_cvt_pk_bf16_f32 v13, v68, v69
	v_lshl_add_u64 v[14:15], v[10:11], 0, v[132:133]
	v_cvt_pk_bf16_f32 v10, v70, v71
	v_cvt_pk_bf16_f32 v11, v72, v73
	v_cvt_pk_bf16_f32 v6, v6, v7
	v_cvt_pk_bf16_f32 v7, v8, v9
	v_cvt_pk_bf16_f32 v8, v2, v3
	s_mov_b32 s36, 1
	v_cvt_pk_bf16_f32 v9, v4, v5
	s_andn2_b64 vcc, exec, s[24:25]
	s_mov_b64 s[0:1], -1
	v_readlane_b32 s77, v254, 61
	global_store_dwordx4 v[136:137], v[128:131], off
	global_store_dwordx4 v[62:63], v[58:61], off
	global_store_dwordx4 v[54:55], v[50:53], off
	global_store_dwordx4 v[46:47], v[42:45], off
	global_store_dwordx4 v[38:39], v[34:37], off
	global_store_dwordx4 v[30:31], v[26:29], off
	global_store_dwordx4 v[22:23], v[18:21], off
	global_store_dwordx4 v[14:15], v[10:13], off
	global_store_dwordx4 v[14:15], v[6:9], off offset:256
	s_cbranch_vccnz .LBB0_277
	s_andn2_b64 vcc, exec, s[12:13]
	s_cbranch_vccnz .LBB0_276
	s_barrier
	s_branch .LBB0_276
